# parallel expert search: 31-step serial LDS chain at each MoE unit start replaced by one LDS read + popcount
# speedup vs baseline: 1.0207x; 1.0207x over previous
.LBB0_744:
	v_mbcnt_lo_u32_b32 v0, -1, 0
	v_mbcnt_hi_u32_b32 v0, -1, v0
	v_min_u32_e32 v0, 30, v0
	v_lshlrev_b32_e32 v0, 2, v0
	v_add_u32_e32 v0, 0x20a44, v0
	ds_read_b32 v0, v0
	s_waitcnt lgkmcnt(0)
	v_cmp_ge_i32_e32 vcc, s5, v0
	s_nop 1
	s_and_b32 s4, vcc_lo, 0x7fffffff
	s_bcnt1_i32_b32 s4, s4
	v_mov_b32_e32 v0, s4

.LBB0_785:
	s_add_i32 s52, s76, 1
	s_mul_i32 s2, s52, s96
	s_add_i32 s2, s57, s2
	s_cmp_lt_i32 s2, s43
	s_cselect_b64 s[24:25], -1, 0
	s_cmp_ge_i32 s2, s43
	s_cselect_b64 s[26:27], -1, 0
	s_and_b64 vcc, exec, s[26:27]
	s_cbranch_vccnz .LBB0_818
	v_mbcnt_lo_u32_b32 v0, -1, 0
	v_mbcnt_hi_u32_b32 v0, -1, v0
	v_min_u32_e32 v0, 30, v0
	v_lshlrev_b32_e32 v0, 2, v0
	v_add_u32_e32 v0, 0x20a44, v0
	ds_read_b32 v0, v0
	s_waitcnt lgkmcnt(0)
	v_cmp_ge_i32_e32 vcc, s2, v0
	s_nop 1
	s_and_b32 s3, vcc_lo, 0x7fffffff
	s_bcnt1_i32_b32 s3, s3
	v_mov_b32_e32 v0, s3

.LBB0_944:
	s_add_u32 s4, s90, 0x8600
	s_addc_u32 s5, s91, 0
	s_ashr_i32 s6, s37, 31
	s_lshr_b32 s6, s6, 23
	s_add_i32 s37, s37, s6
	s_mul_hi_i32 s6, s36, 0x2aaaaaab
	s_lshr_b32 s8, s6, 31
	s_ashr_i32 s43, s6, 2
	s_ashr_i32 s42, s37, 9
	s_add_i32 s43, s43, s8
	s_cmp_lt_i32 s7, s41
	s_cselect_b64 s[12:13], -1, 0
	s_cmp_ge_i32 s7, s41
	s_cbranch_scc1 .LBB0_988
	v_mbcnt_lo_u32_b32 v0, -1, 0
	v_mbcnt_hi_u32_b32 v0, -1, v0
	v_min_u32_e32 v0, 30, v0
	v_lshlrev_b32_e32 v0, 2, v0
	v_add_u32_e32 v0, 0x20a44, v0
	ds_read_b32 v0, v0
	s_waitcnt lgkmcnt(0)
	v_cmp_ge_i32_e32 vcc, s7, v0
	s_nop 1
	s_and_b32 s6, vcc_lo, 0x7fffffff
	s_bcnt1_i32_b32 s6, s6
	v_mov_b32_e32 v0, s6

.LBB0_995:
	s_add_i32 s71, s80, 1
	s_mul_i32 s2, s71, s96
	s_add_i32 s2, s56, s2
	s_cmp_lt_i32 s2, s41
	s_cselect_b64 s[24:25], -1, 0
	s_cmp_ge_i32 s2, s41
	s_cselect_b64 s[26:27], -1, 0
	s_and_b64 vcc, exec, s[26:27]
	s_cbranch_vccnz .LBB0_1041
	v_mbcnt_lo_u32_b32 v0, -1, 0
	v_mbcnt_hi_u32_b32 v0, -1, v0
	v_min_u32_e32 v0, 30, v0
	v_lshlrev_b32_e32 v0, 2, v0
	v_add_u32_e32 v0, 0x20a44, v0
	ds_read_b32 v0, v0
	s_waitcnt lgkmcnt(0)
	v_cmp_ge_i32_e32 vcc, s2, v0
	s_nop 1
	s_and_b32 s3, vcc_lo, 0x7fffffff
	s_bcnt1_i32_b32 s3, s3
	v_mov_b32_e32 v0, s3
